# final combine+LayerNorm phase: gain/bias quads resident in unused registers (loaded once before the row loop) instead of four waited load groups per row
# speedup vs baseline: 1.0052x; 1.0052x over previous
; #define CMB_META(mm, M) do { const int _e0 = tok_e[2 * (mm)], _e1 = tok_e[2 * (mm) + 1]; (M).p0 = (size_t)pblk[_e0] * 256 + tok_p[2 * (mm)]; (M).p1 = (size_t)pblk[_e1] * 256 + tok_p[2 * (mm) + 1]; \
;         (M).h0 = tok_g[2 * (mm)] * (1.0f / 16.0f); (M).h1 = tok_g[2 * (mm) + 1] * (1.0f / 16.0f); } while (0)
; #define CMB_ROWS(mm, M, R) do { _Pragma("unroll") for (int i = 0; i < 4; ++i) { const int col = 8 * lane + 512 * i; (R).xa[i] = *(const u32x4*)(x1b + (size_t)(mm) * DM + col); \
;         (R).ya[i] = *(const u32x2*)((const unsigned char*)Yr + (M).p0 * DM + col); (R).yb[i] = *(const u32x2*)((const unsigned char*)Yr + (M).p1 * DM + col); } } while (0)
; #define CMB_PAIR(j, W, SEL) do { const f32x2 a2 = __builtin_amdgcn_cvt_pk_f32_fp8((int)aw[W], SEL), b2 = __builtin_amdgcn_cvt_pk_f32_fp8((int)bw[W], SEL); \
;                     v[i * 8 + 2 * (j)] = ALPHA * bflo(xw[j]) + h0 * a2[0] + h1 * b2[0]; v[i * 8 + 2 * (j) + 1] = ALPHA * bfhi(xw[j]) + h0 * a2[1] + h1 * b2[1]; \
;                     s += v[i * 8 + 2 * (j)] + v[i * 8 + 2 * (j) + 1]; } while (0)
; template <bool FINAL> ...
;     ...
;     const int mstep = G * 8, m0 = bid * 8 + wid;
;     Meta Mc, Mn; Rows Rc, Rn;
;     Mc.p0 = Mc.p1 = 0; Mc.h0 = Mc.h1 = 0.f; Mn = Mc;
;     if (m0 < T_) { CMB_META(m0, Mc); CMB_ROWS(m0, Mc, Rc); }
;     if (m0 + mstep < T_) CMB_META(m0 + mstep, Mn);
;     Rn = Rc;
;     for (int m = m0; m < T_; m += mstep) {
;         Meta Mnn = Mn;
;         if (m + mstep < T_) CMB_ROWS(m + mstep, Mn, Rn);
;         if (m + 2 * mstep < T_) CMB_META(m + 2 * mstep, Mnn);
;         const float h0 = Mc.h0, h1 = Mc.h1;
;         float v[32]; float s = 0.f;
; #pragma unroll
;         for (int i = 0; i < 4; ++i) {
;             const unsigned xw[4] = {Rc.xa[i].x, Rc.xa[i].y, Rc.xa[i].z, Rc.xa[i].w}; const unsigned aw[2] = {Rc.ya[i].x, Rc.ya[i].y}, bw[2] = {Rc.yb[i].x, Rc.yb[i].y};
;     ...
;             CMB_PAIR(0, 0, false); CMB_PAIR(1, 0, true); CMB_PAIR(2, 1, false); CMB_PAIR(3, 1, true);
;     ...
;         }
;     ...
;             const f32x4 ga = *(const f32x4*)(g + col), gb = *(const f32x4*)(g + col + 4), ba = *(const f32x4*)(bb + col), bbv = *(const f32x4*)(bb + col + 4);
.LBB0_1089:
	s_andn2_b64 vcc, exec, s[0:1]
	s_cbranch_vccnz .LBB0_1096
	s_ashr_i32 s49, s48, 31
	s_lshl_b64 s[0:1], s[48:49], 13
	v_lshlrev_b32_e32 v18, 5, v16
	s_add_u32 s0, s40, s0
	v_mov_b32_e32 v19, v233
	v_or_b32_e32 v20, 0x1000, v18
	v_mov_b32_e32 v21, v233
	s_addc_u32 s1, s41, s1
	v_lshl_add_u64 v[38:39], s[44:45], 0, v[18:19]
	v_lshl_add_u64 v[40:41], s[46:47], 0, v[18:19]
	v_lshl_add_u64 v[42:43], s[44:45], 0, v[20:21]
	v_lshl_add_u64 v[44:45], s[46:47], 0, v[20:21]
	v_or_b32_e32 v20, 0x1800, v18
	v_lshl_add_u64 v[18:19], s[0:1], 0, v[18:19]
	s_mov_b64 s[0:1], 0x1000
	v_lshl_add_u64 v[54:55], v[18:19], 0, s[0:1]
	v_readlane_b32 s0, v254, 6
	s_add_i32 s0, s0, s8
	s_ashr_i32 s1, s0, 31
	s_lshl_b64 s[0:1], s[0:1], 12
	v_lshlrev_b32_e32 v232, 3, v16
	s_add_u32 s0, s58, s0
	v_lshl_add_u64 v[50:51], s[2:3], 0, v[232:233]
	v_lshlrev_b32_e32 v232, 4, v16
	s_addc_u32 s1, s59, s1
	v_lshl_add_u64 v[56:57], s[0:1], 0, v[232:233]
	v_readlane_b32 s0, v254, 50
	v_lshl_add_u64 v[46:47], s[44:45], 0, v[20:21]
	v_lshl_add_u64 v[48:49], s[46:47], 0, v[20:21]
	s_add_i32 s0, s0, s8
	s_waitcnt vmcnt(8)
	v_mov_b64_e32 v[30:31], v[6:7]
	v_mov_b64_e32 v[26:27], v[10:11]
	v_mov_b64_e32 v[22:23], v[14:15]
	v_mov_b64_e32 v[16:17], v[32:33]
	v_mov_b32_e32 v37, v36
	v_readlane_b32 s49, v255, 49
	s_lshl_b32 s0, s0, 1
	s_waitcnt vmcnt(0)
	v_mov_b64_e32 v[58:59], v[76:77]
	v_mov_b64_e32 v[60:61], v[80:81]
	v_mov_b64_e32 v[62:63], v[84:85]
	v_mov_b64_e32 v[64:65], v[88:89]
	v_mov_b64_e32 v[66:67], v[78:79]
	v_mov_b64_e32 v[68:69], v[82:83]
	v_mov_b64_e32 v[70:71], v[86:87]
	v_mov_b64_e32 v[72:73], v[90:91]
	v_mov_b64_e32 v[28:29], v[4:5]
	v_mov_b64_e32 v[24:25], v[8:9]
	v_mov_b64_e32 v[20:21], v[12:13]
	v_mov_b64_e32 v[18:19], v[34:35]
	global_load_dwordx4 v[144:147], v[38:39], off offset:16
	global_load_dwordx4 v[148:151], v[38:39], off
	global_load_dwordx4 v[152:155], v[40:41], off offset:16
	global_load_dwordx4 v[156:159], v[40:41], off
	global_load_dwordx4 v[160:163], v[40:41], off offset:2048
	global_load_dwordx4 v[164:167], v[38:39], off offset:2048
	global_load_dwordx4 v[168:171], v[38:39], off offset:2064
	global_load_dwordx4 v[172:175], v[40:41], off offset:2064
	global_load_dwordx4 v[176:179], v[44:45], off
	global_load_dwordx4 v[180:183], v[42:43], off
	global_load_dwordx4 v[184:187], v[42:43], off offset:16
	global_load_dwordx4 v[188:191], v[44:45], off offset:16
	global_load_dwordx4 v[192:195], v[48:49], off
	global_load_dwordx4 v[196:199], v[46:47], off
	global_load_dwordx4 v[200:203], v[46:47], off offset:16
	global_load_dwordx4 v[204:207], v[48:49], off offset:16
	s_branch .LBB0_1092
.LBB0_1091:
	v_cvt_pk_f32_fp8_e32 v[94:95], v90
	v_cvt_pk_f32_fp8_e32 v[96:97], v88
	v_cvt_pk_f32_fp8_sdwa v[98:99], v90 src0_sel:WORD_1
	v_lshlrev_b32_e32 v142, 16, v32
	v_and_b32_e32 v143, 0xffff0000, v32
	v_pk_mul_f32 v[94:95], v[52:53], v[94:95] op_sel_hi:[0,1]
	v_pk_fma_f32 v[94:95], v[36:37], v[142:143], v[94:95]
	v_cvt_pk_f32_fp8_sdwa v[100:101], v88 src0_sel:WORD_1
	v_pk_fma_f32 v[94:95], v[52:53], v[96:97], v[94:95] op_sel:[1,0,0]
	v_cvt_pk_f32_fp8_e32 v[102:103], v91
	v_add_f32_e32 v32, v95, v94
	v_add_f32_e32 v142, 0, v32
	v_lshlrev_b32_e32 v32, 16, v33
	v_and_b32_e32 v33, 0xffff0000, v33
	v_pk_mul_f32 v[96:97], v[52:53], v[98:99] op_sel_hi:[0,1]
	v_pk_fma_f32 v[32:33], v[36:37], v[32:33], v[96:97]
	v_cvt_pk_f32_fp8_e32 v[104:105], v89
	v_pk_fma_f32 v[96:97], v[52:53], v[100:101], v[32:33] op_sel:[1,0,0]
	v_cvt_pk_f32_fp8_sdwa v[90:91], v91 src0_sel:WORD_1
	v_add_f32_e32 v32, v97, v96
	v_add_f32_e32 v100, v142, v32
	v_lshlrev_b32_e32 v32, 16, v34
	v_and_b32_e32 v33, 0xffff0000, v34
	v_pk_mul_f32 v[98:99], v[52:53], v[102:103] op_sel_hi:[0,1]
	v_pk_fma_f32 v[32:33], v[36:37], v[32:33], v[98:99]
	v_cvt_pk_f32_fp8_sdwa v[88:89], v89 src0_sel:WORD_1
	v_pk_fma_f32 v[98:99], v[52:53], v[104:105], v[32:33] op_sel:[1,0,0]
	v_cvt_pk_f32_fp8_e32 v[106:107], v86
	v_add_f32_e32 v32, v99, v98
	v_add_f32_e32 v100, v100, v32
	v_lshlrev_b32_e32 v32, 16, v35
	v_and_b32_e32 v33, 0xffff0000, v35
	v_pk_mul_f32 v[34:35], v[52:53], v[90:91] op_sel_hi:[0,1]
	v_pk_fma_f32 v[32:33], v[36:37], v[32:33], v[34:35]
	v_cvt_pk_f32_fp8_e32 v[108:109], v84
	v_pk_fma_f32 v[88:89], v[52:53], v[88:89], v[32:33] op_sel:[1,0,0]
	v_cvt_pk_f32_fp8_sdwa v[110:111], v86 src0_sel:WORD_1
	v_add_f32_e32 v32, v89, v88
	v_add_f32_e32 v100, v100, v32
	v_lshlrev_b32_e32 v32, 16, v12
	v_and_b32_e32 v33, 0xffff0000, v12
	v_pk_mul_f32 v[34:35], v[52:53], v[106:107] op_sel_hi:[0,1]
	v_pk_fma_f32 v[32:33], v[36:37], v[32:33], v[34:35]
	v_cvt_pk_f32_fp8_sdwa v[112:113], v84 src0_sel:WORD_1
	v_pk_fma_f32 v[90:91], v[52:53], v[108:109], v[32:33] op_sel:[1,0,0]
	v_cvt_pk_f32_fp8_e32 v[114:115], v87
	v_add_f32_e32 v12, v91, v90
	v_add_f32_e32 v34, v100, v12
	v_lshlrev_b32_e32 v12, 16, v13
	v_and_b32_e32 v13, 0xffff0000, v13
	v_pk_mul_f32 v[32:33], v[52:53], v[110:111] op_sel_hi:[0,1]
	v_pk_fma_f32 v[12:13], v[36:37], v[12:13], v[32:33]
	v_cvt_pk_f32_fp8_e32 v[116:117], v85
	v_pk_fma_f32 v[100:101], v[52:53], v[112:113], v[12:13] op_sel:[1,0,0]
	v_cvt_pk_f32_fp8_sdwa v[86:87], v87 src0_sel:WORD_1
	v_add_f32_e32 v12, v101, v100
	v_add_f32_e32 v34, v34, v12
	v_lshlrev_b32_e32 v12, 16, v14
	v_and_b32_e32 v13, 0xffff0000, v14
	v_pk_mul_f32 v[32:33], v[52:53], v[114:115] op_sel_hi:[0,1]
	v_pk_fma_f32 v[12:13], v[36:37], v[12:13], v[32:33]
	v_cvt_pk_f32_fp8_sdwa v[84:85], v85 src0_sel:WORD_1
	v_pk_fma_f32 v[102:103], v[52:53], v[116:117], v[12:13] op_sel:[1,0,0]
	v_cvt_pk_f32_fp8_e32 v[118:119], v82
	v_add_f32_e32 v12, v103, v102
	v_add_f32_e32 v32, v34, v12
	v_lshlrev_b32_e32 v12, 16, v15
	v_and_b32_e32 v13, 0xffff0000, v15
; #define CMB_PAIR(j, W, SEL) do { const f32x2 a2 = __builtin_amdgcn_cvt_pk_f32_fp8((int)aw[W], SEL), b2 = __builtin_amdgcn_cvt_pk_f32_fp8((int)bw[W], SEL); \
;                     v[i * 8 + 2 * (j)] = ALPHA * bflo(xw[j]) + h0 * a2[0] + h1 * b2[0]; v[i * 8 + 2 * (j) + 1] = ALPHA * bfhi(xw[j]) + h0 * a2[1] + h1 * b2[1]; \
;                     s += v[i * 8 + 2 * (j)] + v[i * 8 + 2 * (j) + 1]; } while (0)
; template <bool FINAL> ...
;     ...
;         for (int i = 0; i < 4; ++i) {
;             const unsigned xw[4] = {Rc.xa[i].x, Rc.xa[i].y, Rc.xa[i].z, Rc.xa[i].w}; const unsigned aw[2] = {Rc.ya[i].x, Rc.ya[i].y}, bw[2] = {Rc.yb[i].x, Rc.yb[i].y};
;     ...
;             CMB_PAIR(0, 0, false); CMB_PAIR(1, 0, true); CMB_PAIR(2, 1, false); CMB_PAIR(3, 1, true);
;     ...
;         }
;         Mc = Mn; Mn = Mnn; Rc = Rn;
;         const float mean = wave_sum(s) * (1.0f / DM); float q = 0.f;
; #pragma unroll
;         for (int i = 0; i < 32; ++i) { const float d = v[i] - mean; q += d * d; }
	v_pk_mul_f32 v[14:15], v[52:53], v[86:87] op_sel_hi:[0,1]
	v_pk_fma_f32 v[12:13], v[36:37], v[12:13], v[14:15]
	v_cvt_pk_f32_fp8_e32 v[120:121], v80
	v_pk_fma_f32 v[84:85], v[52:53], v[84:85], v[12:13] op_sel:[1,0,0]
	v_cvt_pk_f32_fp8_sdwa v[122:123], v82 src0_sel:WORD_1
	v_add_f32_e32 v12, v85, v84
	v_add_f32_e32 v32, v32, v12
	v_lshlrev_b32_e32 v12, 16, v8
	v_and_b32_e32 v13, 0xffff0000, v8
	v_pk_mul_f32 v[14:15], v[52:53], v[118:119] op_sel_hi:[0,1]
	v_pk_fma_f32 v[12:13], v[36:37], v[12:13], v[14:15]
	v_cvt_pk_f32_fp8_sdwa v[124:125], v80 src0_sel:WORD_1
	v_pk_fma_f32 v[86:87], v[52:53], v[120:121], v[12:13] op_sel:[1,0,0]
	v_cvt_pk_f32_fp8_e32 v[126:127], v83
	v_add_f32_e32 v8, v87, v86
	v_add_f32_e32 v14, v32, v8
	v_lshlrev_b32_e32 v8, 16, v9
	v_and_b32_e32 v9, 0xffff0000, v9
	v_pk_mul_f32 v[12:13], v[52:53], v[122:123] op_sel_hi:[0,1]
	v_pk_fma_f32 v[8:9], v[36:37], v[8:9], v[12:13]
	v_cvt_pk_f32_fp8_e32 v[128:129], v81
	v_pk_fma_f32 v[104:105], v[52:53], v[124:125], v[8:9] op_sel:[1,0,0]
	v_cvt_pk_f32_fp8_sdwa v[82:83], v83 src0_sel:WORD_1
	v_add_f32_e32 v8, v105, v104
	v_add_f32_e32 v14, v14, v8
	v_lshlrev_b32_e32 v8, 16, v10
	v_and_b32_e32 v9, 0xffff0000, v10
	v_pk_mul_f32 v[12:13], v[52:53], v[126:127] op_sel_hi:[0,1]
	v_pk_fma_f32 v[8:9], v[36:37], v[8:9], v[12:13]
	v_cvt_pk_f32_fp8_sdwa v[80:81], v81 src0_sel:WORD_1
	v_pk_fma_f32 v[106:107], v[52:53], v[128:129], v[8:9] op_sel:[1,0,0]
	v_cvt_pk_f32_fp8_e32 v[130:131], v78
	v_add_f32_e32 v8, v107, v106
	v_add_f32_e32 v12, v14, v8
	v_lshlrev_b32_e32 v8, 16, v11
	v_and_b32_e32 v9, 0xffff0000, v11
	v_pk_mul_f32 v[10:11], v[52:53], v[82:83] op_sel_hi:[0,1]
	v_pk_fma_f32 v[8:9], v[36:37], v[8:9], v[10:11]
	v_cvt_pk_f32_fp8_e32 v[132:133], v76
	v_pk_fma_f32 v[80:81], v[52:53], v[80:81], v[8:9] op_sel:[1,0,0]
	v_cvt_pk_f32_fp8_sdwa v[134:135], v78 src0_sel:WORD_1
	v_add_f32_e32 v8, v81, v80
	v_add_f32_e32 v12, v12, v8
	v_lshlrev_b32_e32 v8, 16, v4
	v_and_b32_e32 v9, 0xffff0000, v4
	v_pk_mul_f32 v[10:11], v[52:53], v[130:131] op_sel_hi:[0,1]
	v_pk_fma_f32 v[8:9], v[36:37], v[8:9], v[10:11]
	v_cvt_pk_f32_fp8_sdwa v[136:137], v76 src0_sel:WORD_1
	v_pk_fma_f32 v[82:83], v[52:53], v[132:133], v[8:9] op_sel:[1,0,0]
	v_cvt_pk_f32_fp8_e32 v[138:139], v79
	v_add_f32_e32 v4, v83, v82
	v_add_f32_e32 v10, v12, v4
	v_lshlrev_b32_e32 v4, 16, v5
	v_and_b32_e32 v5, 0xffff0000, v5
	v_pk_mul_f32 v[8:9], v[52:53], v[134:135] op_sel_hi:[0,1]
	v_pk_fma_f32 v[4:5], v[36:37], v[4:5], v[8:9]
	v_cvt_pk_f32_fp8_e32 v[140:141], v77
	v_pk_fma_f32 v[108:109], v[52:53], v[136:137], v[4:5] op_sel:[1,0,0]
	v_cvt_pk_f32_fp8_sdwa v[78:79], v79 src0_sel:WORD_1
	v_add_f32_e32 v4, v109, v108
	v_add_f32_e32 v10, v10, v4
	v_lshlrev_b32_e32 v4, 16, v6
	v_and_b32_e32 v5, 0xffff0000, v6
	v_pk_mul_f32 v[8:9], v[52:53], v[138:139] op_sel_hi:[0,1]
	v_pk_fma_f32 v[4:5], v[36:37], v[4:5], v[8:9]
	v_cvt_pk_f32_fp8_sdwa v[76:77], v77 src0_sel:WORD_1
	v_pk_fma_f32 v[110:111], v[52:53], v[140:141], v[4:5] op_sel:[1,0,0]
	v_and_b32_e32 v5, 0xffff0000, v7
	v_add_f32_e32 v4, v111, v110
	v_add_f32_e32 v8, v10, v4
	v_lshlrev_b32_e32 v4, 16, v7
	v_pk_mul_f32 v[6:7], v[52:53], v[78:79] op_sel_hi:[0,1]
	v_pk_fma_f32 v[4:5], v[36:37], v[4:5], v[6:7]
	v_readlane_b32 s8, v255, 25
	v_pk_fma_f32 v[52:53], v[52:53], v[76:77], v[4:5] op_sel:[1,0,0]
	v_readlane_b32 s9, v255, 26
	v_add_f32_e32 v4, v53, v52
	v_add_f32_e32 v4, v8, v4
	ds_swizzle_b32 v5, v4 offset:swizzle(SWAP,1)
	v_lshl_add_u64 v[56:57], v[56:57], 0, s[8:9]
	s_add_i32 s0, s0, s80
	s_mov_b32 s48, s15
	s_waitcnt lgkmcnt(0)
	v_add_f32_e32 v4, v4, v5
	ds_swizzle_b32 v5, v4 offset:swizzle(SWAP,2)
	s_waitcnt lgkmcnt(0)
	v_add_f32_e32 v4, v4, v5
	ds_swizzle_b32 v5, v4 offset:swizzle(SWAP,4)
	s_waitcnt lgkmcnt(0)
	v_add_f32_e32 v4, v4, v5
	ds_swizzle_b32 v5, v4 offset:swizzle(SWAP,8)
	s_waitcnt lgkmcnt(0)
	v_add_f32_e32 v76, v4, v5
	ds_swizzle_b32 v77, v76 offset:swizzle(SWAP,16)
	s_nop 0
	s_nop 0
	s_nop 0
	s_nop 0
	s_waitcnt lgkmcnt(0)
	v_add_f32_e32 v76, v76, v77
	v_mov_b32_e32 v77, v76
	s_nop 1
	v_permlane32_swap_b32_e32 v76, v77
	v_add_f32_e32 v76, v76, v77
	v_mul_f32_e32 v76, 0x3a000000, v76
	v_pk_add_f32 v[78:79], v[94:95], v[76:77] op_sel_hi:[1,0] neg_lo:[0,1] neg_hi:[0,1]
	v_pk_add_f32 v[96:97], v[96:97], v[76:77] op_sel_hi:[1,0] neg_lo:[0,1] neg_hi:[0,1]
	v_pk_mul_f32 v[94:95], v[78:79], v[78:79]
	v_pk_mul_f32 v[112:113], v[96:97], v[96:97]
	v_add_f32_e32 v94, v94, v95
	v_pk_add_f32 v[98:99], v[98:99], v[76:77] op_sel_hi:[1,0] neg_lo:[0,1] neg_hi:[0,1]
	v_add_f32_e32 v94, v112, v94
	v_pk_mul_f32 v[114:115], v[98:99], v[98:99]
	v_add_f32_e32 v94, v113, v94
	v_pk_add_f32 v[88:89], v[88:89], v[76:77] op_sel_hi:[1,0] neg_lo:[0,1] neg_hi:[0,1]
	v_add_f32_e32 v94, v114, v94
	v_pk_mul_f32 v[116:117], v[88:89], v[88:89]
	v_add_f32_e32 v94, v115, v94
	v_pk_add_f32 v[90:91], v[90:91], v[76:77] op_sel_hi:[1,0] neg_lo:[0,1] neg_hi:[0,1]
	v_add_f32_e32 v94, v116, v94
	v_pk_mul_f32 v[118:119], v[90:91], v[90:91]
	v_add_f32_e32 v94, v117, v94
	v_pk_add_f32 v[100:101], v[100:101], v[76:77] op_sel_hi:[1,0] neg_lo:[0,1] neg_hi:[0,1]
	v_add_f32_e32 v94, v118, v94
	v_pk_mul_f32 v[120:121], v[100:101], v[100:101]
	v_add_f32_e32 v94, v119, v94
	v_pk_add_f32 v[102:103], v[102:103], v[76:77] op_sel_hi:[1,0] neg_lo:[0,1] neg_hi:[0,1]
	v_add_f32_e32 v94, v120, v94
	v_pk_mul_f32 v[122:123], v[102:103], v[102:103]
	v_add_f32_e32 v94, v121, v94
	v_pk_add_f32 v[84:85], v[84:85], v[76:77] op_sel_hi:[1,0] neg_lo:[0,1] neg_hi:[0,1]
	v_add_f32_e32 v94, v122, v94
	v_pk_mul_f32 v[124:125], v[84:85], v[84:85]
	v_add_f32_e32 v94, v123, v94
	v_pk_add_f32 v[86:87], v[86:87], v[76:77] op_sel_hi:[1,0] neg_lo:[0,1] neg_hi:[0,1]
; __device__ __forceinline__ unsigned cvtpk(float lo, float hi) { unsigned r; asm volatile("v_cvt_pk_bf16_f32 %0, %1, %2" : "=v"(r) : "v"(lo), "v"(hi)); return r; }
; template <bool FINAL> ...
;     ...
;         const float mean = wave_sum(s) * (1.0f / DM); float q = 0.f;
; #pragma unroll
;         for (int i = 0; i < 32; ++i) { const float d = v[i] - mean; q += d * d; }
;         const float rstd = rsqrtf(wave_sum(q) * (1.0f / DM) + 1e-5f);
; #pragma unroll
;         for (int i = 0; i < 4; ++i) { const int col = 8 * lane + 512 * i;
;             const f32x4 ga = *(const f32x4*)(g + col), gb = *(const f32x4*)(g + col + 4), ba = *(const f32x4*)(bb + col), bbv = *(const f32x4*)(bb + col + 4);
;             float y[8];
; #pragma unroll
;             for (int j = 0; j < 4; ++j) { y[j] = (v[i * 8 + j] - mean) * rstd * ga[j] + ba[j]; y[4 + j] = (v[i * 8 + 4 + j] - mean) * rstd * gb[j] + bbv[j]; }
;     ...
;             if (dbg_bad) { for (int j = 0; j < 8; ++j) y[j] = 0.f; }
;     ...
;             if constexpr (FINAL) { *(f32x4*)(fo + (size_t)m * DM + col) = (f32x4){y[0], y[1], y[2], y[3]}; *(f32x4*)(fo + (size_t)m * DM + col + 4) = (f32x4){y[4], y[5], y[6], y[7]}; }
;             else { *(u32x4*)(xo + (size_t)m * DM + col) = (u32x4){cvtpk(y[0], y[1]), cvtpk(y[2], y[3]), cvtpk(y[4], y[5]), cvtpk(y[6], y[7])};
;                 if constexpr (F8_IN) *(u32x2*)(xq + (size_t)m * DM + col) = (u32x2){pk4_fp8(y[0], y[1], y[2], y[3]), pk4_fp8(y[4], y[5], y[6], y[7])}; } }
	v_add_f32_e32 v94, v124, v94
	v_pk_mul_f32 v[126:127], v[86:87], v[86:87]
	v_add_f32_e32 v94, v125, v94
	v_pk_add_f32 v[104:105], v[104:105], v[76:77] op_sel_hi:[1,0] neg_lo:[0,1] neg_hi:[0,1]
	v_add_f32_e32 v94, v126, v94
	v_pk_mul_f32 v[128:129], v[104:105], v[104:105]
	v_add_f32_e32 v94, v127, v94
	v_pk_add_f32 v[106:107], v[106:107], v[76:77] op_sel_hi:[1,0] neg_lo:[0,1] neg_hi:[0,1]
	v_add_f32_e32 v94, v128, v94
	v_pk_mul_f32 v[130:131], v[106:107], v[106:107]
	v_add_f32_e32 v94, v129, v94
	v_pk_add_f32 v[80:81], v[80:81], v[76:77] op_sel_hi:[1,0] neg_lo:[0,1] neg_hi:[0,1]
	v_add_f32_e32 v94, v130, v94
	v_pk_mul_f32 v[132:133], v[80:81], v[80:81]
	v_add_f32_e32 v94, v131, v94
	v_pk_add_f32 v[134:135], v[82:83], v[76:77] op_sel_hi:[1,0] neg_lo:[0,1] neg_hi:[0,1]
	v_add_f32_e32 v94, v132, v94
	v_pk_mul_f32 v[82:83], v[134:135], v[134:135]
	v_add_f32_e32 v94, v133, v94
	v_pk_add_f32 v[136:137], v[108:109], v[76:77] op_sel_hi:[1,0] neg_lo:[0,1] neg_hi:[0,1]
	v_add_f32_e32 v82, v82, v94
	v_pk_mul_f32 v[108:109], v[136:137], v[136:137]
	v_add_f32_e32 v82, v83, v82
	v_pk_add_f32 v[110:111], v[110:111], v[76:77] op_sel_hi:[1,0] neg_lo:[0,1] neg_hi:[0,1]
	v_add_f32_e32 v82, v108, v82
	v_pk_mul_f32 v[138:139], v[110:111], v[110:111]
	v_add_f32_e32 v82, v109, v82
	v_pk_add_f32 v[52:53], v[52:53], v[76:77] op_sel_hi:[1,0] neg_lo:[0,1] neg_hi:[0,1]
	v_add_f32_e32 v82, v138, v82
	v_pk_mul_f32 v[76:77], v[52:53], v[52:53]
	v_add_f32_e32 v82, v139, v82
	v_add_f32_e32 v76, v76, v82
	v_add_f32_e32 v76, v77, v76
	ds_swizzle_b32 v77, v76 offset:swizzle(SWAP, 1)
	s_waitcnt lgkmcnt(0)
	v_add_f32_e32 v76, v76, v77
	ds_swizzle_b32 v77, v76 offset:swizzle(SWAP, 2)
	s_waitcnt lgkmcnt(0)
	v_add_f32_e32 v76, v76, v77
	ds_swizzle_b32 v77, v76 offset:swizzle(SWAP, 4)
	s_waitcnt lgkmcnt(0)
	v_add_f32_e32 v76, v76, v77
	ds_swizzle_b32 v77, v76 offset:swizzle(SWAP, 8)
	s_waitcnt lgkmcnt(0)
	v_add_f32_e32 v76, v76, v77
	ds_swizzle_b32 v77, v76 offset:swizzle(SWAP, 16)
	s_waitcnt lgkmcnt(0)
	v_add_f32_e32 v76, v76, v77
	v_mov_b32_e32 v77, v76
	s_nop 1
	v_permlane32_swap_b32_e32 v76, v77
	v_add_f32_e32 v76, v76, v77
	v_mov_b32_e32 v77, 0x3727c5ac
	v_fmamk_f32 v76, v76, 0x3a000000, v77
	v_mul_f32_e32 v77, 0x4b800000, v76
	v_cmp_gt_f32_e32 vcc, s91, v76
	s_nop 1
	v_cndmask_b32_e32 v76, v76, v77, vcc
	v_rsq_f32_e32 v76, v76
	s_nop 0
	v_mul_f32_e32 v77, 0x45800000, v76
	v_cndmask_b32_e32 v112, v76, v77, vcc
	v_pk_mul_f32 v[76:77], v[78:79], v[112:113] op_sel_hi:[1,0]
	v_pk_mul_f32 v[78:79], v[96:97], v[112:113] op_sel_hi:[1,0]
	s_waitcnt vmcnt(0)
	v_pk_fma_f32 v[8:9], v[148:149], v[76:77], v[156:157]
	v_pk_fma_f32 v[10:11], v[150:151], v[78:79], v[158:159]
	global_store_dwordx4 v[54:55], v[8:11], off offset:-4096
	v_pk_mul_f32 v[76:77], v[100:101], v[112:113] op_sel_hi:[1,0]
	v_pk_mul_f32 v[78:79], v[90:91], v[112:113] op_sel_hi:[1,0]
	v_pk_mul_f32 v[8:9], v[98:99], v[112:113] op_sel_hi:[1,0]
	v_pk_mul_f32 v[10:11], v[88:89], v[112:113] op_sel_hi:[1,0]
	v_pk_fma_f32 v[4:5], v[144:145], v[8:9], v[152:153]
	v_pk_fma_f32 v[6:7], v[146:147], v[10:11], v[154:155]
	global_store_dwordx4 v[54:55], v[4:7], off offset:-4080
	s_nop 0
	s_nop 0
	s_nop 0
	s_nop 0
	s_nop 0
	v_pk_mul_f32 v[80:81], v[80:81], v[112:113] op_sel_hi:[1,0]
	v_pk_mul_f32 v[82:83], v[106:107], v[112:113] op_sel_hi:[1,0]
	s_andn2_b64 vcc, exec, s[6:7]
	v_pk_mul_f32 v[114:115], v[136:137], v[112:113] op_sel_hi:[1,0]
	v_pk_mul_f32 v[116:117], v[134:135], v[112:113] op_sel_hi:[1,0]
	v_readlane_b32 s6, v254, 19
	v_pk_mul_f32 v[52:53], v[52:53], v[112:113] op_sel_hi:[1,0]
	v_pk_mul_f32 v[110:111], v[110:111], v[112:113] op_sel_hi:[1,0]
	v_readlane_b32 s7, v254, 20
	v_mov_b64_e32 v[88:89], v[64:65]
	v_mov_b64_e32 v[90:91], v[72:73]
	v_pk_fma_f32 v[4:5], v[164:165], v[78:79], v[160:161]
	v_pk_fma_f32 v[6:7], v[166:167], v[76:77], v[162:163]
	global_store_dwordx4 v[54:55], v[4:7], off offset:-2048
	v_pk_mul_f32 v[76:77], v[104:105], v[112:113] op_sel_hi:[1,0]
	v_pk_mul_f32 v[78:79], v[86:87], v[112:113] op_sel_hi:[1,0]
	v_pk_mul_f32 v[6:7], v[84:85], v[112:113] op_sel_hi:[1,0]
	v_pk_mul_f32 v[4:5], v[102:103], v[112:113] op_sel_hi:[1,0]
	v_pk_fma_f32 v[6:7], v[170:171], v[6:7], v[174:175]
	v_pk_fma_f32 v[4:5], v[168:169], v[4:5], v[172:173]
	global_store_dwordx4 v[54:55], v[4:7], off offset:-2032
	s_nop 0
	s_nop 0
	s_nop 0
	s_nop 0
	s_nop 0
	v_mov_b64_e32 v[84:85], v[62:63]
	v_mov_b64_e32 v[86:87], v[70:71]
	v_pk_fma_f32 v[4:5], v[78:79], v[180:181], v[176:177]
	v_pk_fma_f32 v[6:7], v[76:77], v[182:183], v[178:179]
	v_pk_fma_f32 v[8:9], v[82:83], v[184:185], v[188:189]
	v_pk_fma_f32 v[10:11], v[80:81], v[186:187], v[190:191]
	global_store_dwordx4 v[54:55], v[4:7], off
	global_store_dwordx4 v[54:55], v[8:11], off offset:16
	s_nop 0
	s_nop 0
	s_nop 0
	s_nop 0
	v_mov_b64_e32 v[4:5], v[28:29]
	v_mov_b64_e32 v[8:9], v[24:25]
	v_mov_b64_e32 v[12:13], v[20:21]
	v_mov_b64_e32 v[34:35], v[18:19]
	v_mov_b64_e32 v[76:77], v[58:59]
	v_mov_b64_e32 v[80:81], v[60:61]
	v_mov_b64_e32 v[78:79], v[66:67]
	v_mov_b64_e32 v[82:83], v[68:69]
	v_mov_b64_e32 v[6:7], v[30:31]
	v_mov_b64_e32 v[10:11], v[26:27]
	v_mov_b64_e32 v[14:15], v[22:23]
	v_mov_b64_e32 v[32:33], v[16:17]
	v_pk_fma_f32 v[94:95], v[116:117], v[196:197], v[192:193]
	v_pk_fma_f32 v[96:97], v[114:115], v[198:199], v[194:195]
	v_pk_fma_f32 v[98:99], v[110:111], v[200:201], v[204:205]
	v_pk_fma_f32 v[100:101], v[52:53], v[202:203], v[206:207]
	global_store_dwordx4 v[54:55], v[94:97], off offset:2048
	global_store_dwordx4 v[54:55], v[98:101], off offset:2064
	v_lshl_add_u64 v[54:55], v[54:55], 0, s[6:7]
	v_mov_b64_e32 v[52:53], v[74:75]
	s_cbranch_vccz .LBB0_1096
